# v69 + plain tiles (8,9) also moved to the weight-converting workgroups (swapped with sigmoid tiles 10,11)
# baseline (speedup 1.0000x reference)
;     __device__ bool next(int i, Unit& u) const { if (!base.next(i >> 1, u)) return false; if (i & 1) { u.pm += MTOK / BM; u.pn += DM / BM; } return true; }
;   __device__ __forceinline__ bool next(int i,AttnUnit&u)const{ if(i>=2||vcu>=256)return false; const int s=vcu&3; u.bh=vcu>>2; u.qb=(i==0)?7-s:s; return true; }
;     __host__ __device__ bool next(int i, Unit& u) const {
;         const int L = i * G + c; if (L >= nwg) return false;
;         int wgid = L; { const int q = nwg / NXCD, r = nwg % NXCD, xcd = wgid % NXCD, off = wgid / NXCD; wgid = (xcd < r ? xcd * (q + 1) : r * (q + 1) + (xcd - r) * q) + off; }
;         const int nig = WGM * nN, gid = wgid / nig, fm = gid * WGM, gsz = (nM - fm) < WGM ? (nM - fm) : WGM;
;         u.pm = fm + ((wgid % nig) % gsz); u.pn = (wgid % nig) / gsz; u.half = 0; return true;
.LBB0_382:
	s_ashr_i32 s4, s21, 31
	s_lshr_b32 s4, s4, 29
	s_add_i32 s4, s21, s4
	s_ashr_i32 s5, s4, 3
	s_and_b32 s4, s4, -8
	s_sub_i32 s4, s21, s4
	s_cmp_lt_i32 s4, 0
	s_movk_i32 s6, 0x91
	s_cselect_b32 s6, s6, 0x90
	s_mul_i32 s4, s4, s6
	s_add_i32 s4, s4, s5
	s_mul_hi_i32 s5, s4, 0x38e38e39
	s_lshr_b32 s6, s5, 31
	s_ashr_i32 s5, s5, 5
	s_add_i32 s5, s5, s6
	s_lshl_b32 s6, s5, 3
	s_mulk_i32 s5, 0x90
	s_sub_i32 s4, s4, s5
	s_bfe_u32 s5, s4, 0x3001c
	s_add_i32 s5, s4, s5
	s_sext_i32_i16 s7, s5
	s_and_b32 s5, s5, 0xfff8
	s_sub_i32 s4, s4, s5
	s_sext_i32_i16 s4, s4
	s_add_i32 s18, s6, s4
	s_ashr_i32 s70, s7, 3
	s_mul_i32 s4, s70, 5
	s_cmp_lt_u32 s70, 12
	s_cbranch_scc0 .Lpn_hi0
	s_mov_b32 s6, 0x86229020
	s_mov_b32 s7, 0x4a16a39
	s_branch .Lpn_go0

;     __device__ bool next(int i, Unit& u) const { if (!base.next(i >> 1, u)) return false; if (i & 1) { u.pm += MTOK / BM; u.pn += DM / BM; } return true; }
;   __device__ __forceinline__ bool next(int i,AttnUnit&u)const{ if(i>=2||vcu>=256)return false; const int s=vcu&3; u.bh=vcu>>2; u.qb=(i==0)?7-s:s; return true; }
;     __host__ __device__ bool next(int i, Unit& u) const {
;         const int L = i * G + c; if (L >= nwg) return false;
;         int wgid = L; { const int q = nwg / NXCD, r = nwg % NXCD, xcd = wgid % NXCD, off = wgid / NXCD; wgid = (xcd < r ? xcd * (q + 1) : r * (q + 1) + (xcd - r) * q) + off; }
;         const int nig = WGM * nN, gid = wgid / nig, fm = gid * WGM, gsz = (nM - fm) < WGM ? (nM - fm) : WGM;
;         u.pm = fm + ((wgid % nig) % gsz); u.pn = (wgid % nig) / gsz; u.half = 0; return true;
; template <class Epi, class Sched, bool ALIGN_EPI = false, bool SP2 = false>
; __device__ __forceinline__ void gemm_phase(PG8_LAS unsigned char* lds, const Gemm g, const Sched& S, const Epi& E) {
;     ...
;         const bool has_next = S.next(ui + 1, nxt);
;         const char* nA = has_next ? (const char*)g.A + (size_t)nxt.pm * tstep + (nxt.half == 2 ? hstep : (size_t)0) : cA; const char* nB = has_next ? (const char*)g.Bt + (size_t)nxt.pn * tstep : cB;
.LBB0_392:
	s_add_i32 s72, s72, 1
	s_mul_i32 s10, s72, s33
	s_add_i32 s10, s10, s21
	s_cmpk_lt_i32 s10, 0x480
	s_cselect_b64 s[64:65], -1, 0
	s_cmpk_gt_i32 s10, 0x47f
	s_cbranch_scc1 .LBB0_394
	s_ashr_i32 s11, s10, 31
	s_lshr_b32 s11, s11, 29
	s_add_i32 s11, s10, s11
	s_ashr_i32 s12, s11, 3
	s_and_b32 s11, s11, -8
	s_sub_i32 s10, s10, s11
	s_cmp_lt_i32 s10, 0
	s_movk_i32 s11, 0x91
	s_cselect_b32 s11, s11, 0x90
	s_mul_i32 s10, s10, s11
	s_add_i32 s10, s10, s12
	s_mul_hi_i32 s11, s10, 0x38e38e39
	s_lshr_b32 s12, s11, 31
	s_ashr_i32 s11, s11, 5
	s_add_i32 s11, s11, s12
	s_lshl_b32 s12, s11, 3
	s_mulk_i32 s11, 0x90
	s_sub_i32 s10, s10, s11
	s_bfe_u32 s11, s10, 0x3001c
	s_add_i32 s11, s10, s11
	s_sext_i32_i16 s13, s11
	s_and_b32 s11, s11, 0xfff8
	s_sub_i32 s10, s10, s11
	s_sext_i32_i16 s10, s10
	s_add_i32 s60, s12, s10
	s_ashr_i32 s62, s13, 3
	s_mul_i32 s10, s62, 5
	s_cmp_lt_u32 s62, 12
	s_cbranch_scc0 .Lpn_hi1
	s_mov_b32 s12, 0x86229020
	s_mov_b32 s13, 0x4a16a39
	s_branch .Lpn_go1
